# speedup vs baseline: 1.1192x; 1.0043x over previous
.LBB0_7:
	s_or_b64 exec, exec, s[4:5]
	s_mov_b32 s34, 0x60441c00
	v_writelane_b32 v20, s34, 0
	s_mov_b32 s34, 0x53371d01
	v_writelane_b32 v20, s34, 1
	s_mov_b32 s34, 0x62461e02
	v_writelane_b32 v20, s34, 2
	s_mov_b32 s34, 0x6f471f03
	v_writelane_b32 v20, s34, 3
	s_mov_b32 s34, 0x78522a0e
	v_writelane_b32 v20, s34, 4
	s_mov_b32 s34, 0x61452b0f
	v_writelane_b32 v20, s34, 5
	s_mov_b32 s34, 0x6e543810
	v_writelane_b32 v20, s34, 6
	s_mov_b32 s34, 0x78553911
	v_writelane_b32 v20, s34, 7
	s_mov_b32 s34, 0x70482c12
	v_writelane_b32 v20, s34, 8
	s_mov_b32 s34, 0x71573b13
	v_writelane_b32 v20, s34, 9
	s_mov_b32 s34, 0x78643c14
	v_writelane_b32 v20, s34, 10
	s_mov_b32 s34, 0x734b2f15
	v_writelane_b32 v20, s34, 11
	s_mov_b32 s34, 0x563a2004
	v_writelane_b32 v20, s34, 12
	s_mov_b32 s34, 0x63492d05
	v_writelane_b32 v20, s34, 13
	s_mov_b32 s34, 0x724a2e06
	v_writelane_b32 v20, s34, 14
	s_mov_b32 s34, 0x653d2107
	v_writelane_b32 v20, s34, 15
	s_mov_b32 s34, 0x74583e22
	v_writelane_b32 v20, s34, 16
	s_mov_b32 s34, 0x78673f23
	v_writelane_b32 v20, s34, 17
	s_mov_b32 s34, 0x765a3216
	v_writelane_b32 v20, s34, 18
	s_mov_b32 s34, 0x775b4125
	v_writelane_b32 v20, s34, 19
	s_mov_b32 s34, 0x664c3008
	v_writelane_b32 v20, s34, 20
	s_mov_b32 s34, 0x75593109
	v_writelane_b32 v20, s34, 21
	s_mov_b32 s34, 0x6840240a
	v_writelane_b32 v20, s34, 22
	s_mov_b32 s34, 0x694d3317
	v_writelane_b32 v20, s34, 23
	s_mov_b32 s34, 0x785c3418
	v_writelane_b32 v20, s34, 24
	s_mov_b32 s34, 0x6b4f270b
	v_writelane_b32 v20, s34, 25
	s_mov_b32 s34, 0x5e42280c
	v_writelane_b32 v20, s34, 26
	s_mov_b32 s34, 0x6d51290d
	v_writelane_b32 v20, s34, 27
	s_mov_b32 s34, 0x786a4e26
	v_writelane_b32 v20, s34, 28
	s_mov_b32 s34, 0x785d3519
	v_writelane_b32 v20, s34, 29
	s_mov_b32 s34, 0x6c50361a
	v_writelane_b32 v20, s34, 30
	s_mov_b32 s34, 0x785f431b
	v_writelane_b32 v20, s34, 31
	s_mov_b32 s34, 0x38587000
	v_writelane_b32 v22, s34, 0
	s_mov_b32 s34, 0xa878
	v_writelane_b32 v23, s34, 0
	s_mov_b32 s34, 0x80482830
	v_writelane_b32 v22, s34, 1
	s_mov_b32 s34, 0xa068
	v_writelane_b32 v23, s34, 1
	s_mov_b32 s34, 0x59790191
	v_writelane_b32 v22, s34, 2
	s_mov_b32 s34, 0x3971
	v_writelane_b32 v23, s34, 2
	s_mov_b32 s34, 0x9949515a
	v_writelane_b32 v22, s34, 3
	s_mov_b32 s34, 0x2969
	v_writelane_b32 v23, s34, 3
	s_mov_b32 s34, 0x222422a
	v_writelane_b32 v22, s34, 4
	s_mov_b32 s34, 0x3a72
	v_writelane_b32 v23, s34, 4
	s_mov_b32 s34, 0x329a1a03
	v_writelane_b32 v22, s34, 5
	s_mov_b32 s34, 0x8a6a
	v_writelane_b32 v23, s34, 5
	s_mov_b32 s34, 0x5b23934b
	v_writelane_b32 v22, s34, 6
	s_mov_b32 s34, 0x3b73
	v_writelane_b32 v23, s34, 6
	s_mov_b32 s34, 0x83541374
	v_writelane_b32 v22, s34, 7
	s_mov_b32 s34, 0x336b
	v_writelane_b32 v23, s34, 7
	s_mov_b32 s34, 0x3c1c2434
	v_writelane_b32 v22, s34, 8
	s_mov_b32 s34, 0x48c
	v_writelane_b32 v23, s34, 8
	s_mov_b32 s34, 0x4c1da455
	v_writelane_b32 v22, s34, 9
	s_mov_b32 s34, 0x449c
	v_writelane_b32 v23, s34, 9
	s_mov_b32 s34, 0x8d25052d
	v_writelane_b32 v22, s34, 10
	s_mov_b32 s34, 0x9d5d
	v_writelane_b32 v23, s34, 10
	s_mov_b32 s34, 0x761e4556
	v_writelane_b32 v22, s34, 11
	s_mov_b32 s34, 0x3565
	v_writelane_b32 v23, s34, 11
	s_mov_b32 s34, 0x46368e6e
	v_writelane_b32 v22, s34, 12
	s_mov_b32 s34, 0x63e
	v_writelane_b32 v23, s34, 12
	s_mov_b32 s34, 0x5f579e77
	v_writelane_b32 v22, s34, 13
	s_mov_b32 s34, 0x2ea6
	v_writelane_b32 v23, s34, 13
	s_mov_b32 s34, 0x174f1f9f
	v_writelane_b32 v22, s34, 14
	s_mov_b32 s34, 0x278f
	v_writelane_b32 v23, s34, 14
	s_mov_b32 s34, 0x38584700
	v_writelane_b32 v22, s34, 15
	s_mov_b32 s34, 0xa897
	v_writelane_b32 v23, s34, 15
	s_mov_b32 s34, 0x90982008
	v_writelane_b32 v22, s34, 16
	s_mov_b32 s34, 0x4060
	v_writelane_b32 v23, s34, 16
	s_mov_b32 s34, 0x411810a1
	v_writelane_b32 v22, s34, 17
	s_mov_b32 s34, 0x5088
	v_writelane_b32 v23, s34, 17
	s_mov_b32 s34, 0x8161197a
	v_writelane_b32 v22, s34, 18
	s_mov_b32 s34, 0x2109
	v_writelane_b32 v23, s34, 18
	s_mov_b32 s34, 0x12314aa2
	v_writelane_b32 v22, s34, 19
	s_mov_b32 s34, 0x1189
	v_writelane_b32 v23, s34, 19
	s_mov_b32 s34, 0x520a430b
	v_writelane_b32 v22, s34, 20
	s_mov_b32 s34, 0x6292
	v_writelane_b32 v23, s34, 20
	s_mov_b32 s34, 0x9b828b53
	v_writelane_b32 v22, s34, 21
	s_mov_b32 s34, 0x2b63
	v_writelane_b32 v23, s34, 21
	s_mov_b32 s34, 0x7c7b5c84
	v_writelane_b32 v22, s34, 22
	s_mov_b32 s34, 0xa31b
	v_writelane_b32 v23, s34, 22
	s_mov_b32 s34, 0x6c0c957d
	v_writelane_b32 v22, s34, 23
	s_mov_b32 s34, 0x942c
	v_writelane_b32 v23, s34, 23
	s_mov_b32 s34, 0x753d85a5
	v_writelane_b32 v22, s34, 24
	s_mov_b32 s34, 0x6414
	v_writelane_b32 v23, s34, 24
	s_mov_b32 s34, 0x5e6d7e26
	v_writelane_b32 v22, s34, 25
	s_mov_b32 s34, 0x4d0d
	v_writelane_b32 v23, s34, 25
	s_mov_b32 s34, 0x8666160f
	v_writelane_b32 v22, s34, 26
	s_mov_b32 s34, 0x9615
	v_writelane_b32 v23, s34, 26
	s_mov_b32 s34, 0x2f7f0787
	v_writelane_b32 v22, s34, 27
	s_mov_b32 s34, 0x4e0e
	v_writelane_b32 v23, s34, 27
	s_mov_b32 s34, 0xa76f2008
	v_writelane_b32 v22, s34, 28
	s_mov_b32 s34, 0x373f
	v_writelane_b32 v23, s34, 28
	s_mov_b32 s34, 0x90982008
	v_writelane_b32 v22, s34, 29
	s_mov_b32 s34, 0x4067
	v_writelane_b32 v23, s34, 29
	s_mov_b32 s34, 0x90982008
	v_writelane_b32 v22, s34, 30
	s_mov_b32 s34, 0x4060
	v_writelane_b32 v23, s34, 30
	s_mov_b32 s34, 0x90982008
	v_writelane_b32 v22, s34, 31
	s_mov_b32 s34, 0x4060
	v_writelane_b32 v23, s34, 31
	s_add_u32 s32, s20, s30
	s_addc_u32 s33, s21, 0
	v_lshlrev_b32_e32 v21, 2, v0
	v_add_u32_e32 v21, 0x21000, v21
	v_cmp_gt_u32_e32 vcc, 32, v0
	s_and_saveexec_b64 s[4:5], vcc
	global_store_dword v21, v20, s[32:33]
	global_store_dword v21, v22, s[32:33] offset:128
	global_store_dword v21, v23, s[32:33] offset:256
	s_or_b64 exec, exec, s[4:5]
	s_mov_b64 s[4:5], 0
